# gate/up epilogue: the full drain covering the next unit's bias preload moved from mid-epilogue to before the first store (no stores pending at the drain)
# speedup vs baseline: 1.0021x; 1.0021x over previous
; __device__ __forceinline__ u32x4 pack8(const f32x4 v0, const f32x4 v1) { u32x4 w; w.x = cvt_pk_bf16(v0[0], v0[1]); w.y = cvt_pk_bf16(v0[2], v0[3]); w.z = cvt_pk_bf16(v1[0], v1[1]); w.w = cvt_pk_bf16(v1[2], v1[3]); return w; }
;     __device__ __forceinline__ void operator()(const f32x4 (&acc)[2][2][4][2], const Unit& u, int wr, int wc, int fr, int fq) const {
;         const int row0 = u.pm * BM + wr * 64 + fr, f0 = u.pn * HALF + wc * 32 + 8 * fq;
; #pragma unroll
;         for (int ai = 0; ai < 2; ++ai)
; #pragma unroll
;             for (int m = 0; m < 4; ++m) {
;                 f32x4 o[2];
; #pragma unroll
;                 for (int n = 0; n < 2; ++n) { const f32x4 g4 = acc[ai][0][m][n], u4 = acc[ai][1][m][n];
; #pragma unroll
;                     for (int i = 0; i < 4; i += 2) {
;                         typedef float f32x2p __attribute__((ext_vector_type(2)));
;                         const f32x2p g = {__builtin_amdgcn_fmed3f(g4[i], -3.0e38f, 7.0f), __builtin_amdgcn_fmed3f(g4[i + 1], -3.0e38f, 7.0f)}, up = {__builtin_amdgcn_fmed3f(u4[i], -7.0f, 7.0f), __builtin_amdgcn_fmed3f(u4[i + 1], -7.0f, 7.0f)};
;                         const f32x2p a = g * (f32x2p){-1.702f * 1.4426950408889634f, -1.702f * 1.4426950408889634f};
;                         const f32x2p d = (f32x2p){__builtin_amdgcn_exp2f(a.x), __builtin_amdgcn_exp2f(a.y)} + (f32x2p){1.0f, 1.0f};
;                         const f32x2p t = g * (f32x2p){__builtin_amdgcn_rcpf(d.x), __builtin_amdgcn_rcpf(d.y)};
;                         const f32x2p r = __builtin_elementwise_fma(t, up, t); o[n][i] = r.x; o[n][i + 1] = r.y; } }
;                 *(u32x4*)(ACT + (size_t)(row0 + ai * HALF + m * 16) * 1024 + f0) = pack8(o[0], o[1]); }
.LBB0_1099:
	s_add_u32 s8, s21, 0xffffff00
	s_addc_u32 s9, s37, -1
	s_ashr_i32 s69, s68, 31
	s_lshl_b64 s[10:11], s[68:69], 13
	s_add_u32 s2, s75, s10
	s_addc_u32 s12, s50, s11
	s_lshl_b32 s10, s63, 7
	s_ashr_i32 s11, s10, 31
	s_lshl_b64 s[10:11], s[10:11], 2
	s_add_u32 s2, s2, s10
	s_addc_u32 s11, s12, s11
	s_add_u32 s10, s2, s42
	s_addc_u32 s11, s11, 0
	v_mov_b32_e32 v147, v1
	v_lshl_add_u64 v[138:139], s[10:11], 0, v[146:147]
	global_load_dwordx4 v[130:133], v146, s[10:11] offset:16
	global_load_dwordx4 v[134:137], v146, s[10:11]
	s_mov_b64 s[10:11], 0x1000
	s_movk_i32 s2, 0x1000
	v_lshl_add_u64 v[140:141], v[138:139], 0, s[10:11]
	v_add_co_u32_e32 v138, vcc, s2, v138
	s_nop 1
	v_addc_co_u32_e32 v139, vcc, 0, v139, vcc
	global_load_dwordx4 v[142:145], v[138:139], off
	s_nop 0
	global_load_dwordx4 v[138:141], v[140:141], off offset:16
	v_med3_f32 v166, v122, s57, v234
	v_med3_f32 v167, v123, s57, v234
	v_pk_mul_f32 v[182:183], v[166:167], s[96:97] op_sel_hi:[1,0]
	v_med3_f32 v180, v78, s33, v234
	v_exp_f32_e32 v182, v182
	v_exp_f32_e32 v183, v183
	v_med3_f32 v181, v79, s33, v234
	v_lshl_add_u32 v164, s62, 8, v153
	v_lshl_or_b32 v162, s90, 7, v179
	v_pk_add_f32 v[182:183], v[182:183], 1.0 op_sel_hi:[1,0]
	v_ashrrev_i32_e32 v165, 31, v164
	v_rcp_f32_e32 v182, v182
	v_rcp_f32_e32 v183, v183
	v_ashrrev_i32_e32 v163, 31, v162
	s_mov_b32 s2, 0x40000
	v_pk_mul_f32 v[166:167], v[166:167], v[182:183]
	s_nop 0
	v_pk_fma_f32 v[166:167], v[166:167], v[180:181], v[166:167]
	v_med3_f32 v180, v124, s57, v234
	v_med3_f32 v181, v125, s57, v234
	v_pk_mul_f32 v[188:189], v[180:181], s[96:97] op_sel_hi:[1,0]
	v_med3_f32 v182, v80, s33, v234
	v_exp_f32_e32 v188, v188
	v_exp_f32_e32 v189, v189
	v_med3_f32 v183, v81, s33, v234
	v_pk_add_f32 v[188:189], v[188:189], 1.0 op_sel_hi:[1,0]
	s_nop 0
	v_rcp_f32_e32 v188, v188
	v_rcp_f32_e32 v189, v189
	s_nop 0
	v_pk_mul_f32 v[180:181], v[180:181], v[188:189]
	s_nop 0
	v_pk_fma_f32 v[182:183], v[180:181], v[182:183], v[180:181]
	v_med3_f32 v180, v114, s57, v234
	v_med3_f32 v181, v115, s57, v234
	v_pk_mul_f32 v[190:191], v[180:181], s[96:97] op_sel_hi:[1,0]
	v_med3_f32 v188, v74, s33, v234
	v_exp_f32_e32 v190, v190
	v_exp_f32_e32 v191, v191
	v_med3_f32 v189, v75, s33, v234
	v_pk_add_f32 v[190:191], v[190:191], 1.0 op_sel_hi:[1,0]
	s_nop 0
	v_rcp_f32_e32 v190, v190
	v_rcp_f32_e32 v191, v191
	s_nop 0
	v_pk_mul_f32 v[180:181], v[180:181], v[190:191]
	s_nop 0
	v_pk_fma_f32 v[188:189], v[180:181], v[188:189], v[180:181]
	v_med3_f32 v180, v116, s57, v234
	v_med3_f32 v181, v117, s57, v234
	v_pk_mul_f32 v[192:193], v[180:181], s[96:97] op_sel_hi:[1,0]
	v_med3_f32 v190, v76, s33, v234
	v_exp_f32_e32 v192, v192
	v_exp_f32_e32 v193, v193
	v_med3_f32 v191, v77, s33, v234
	v_pk_add_f32 v[192:193], v[192:193], 1.0 op_sel_hi:[1,0]
	s_nop 0
	v_rcp_f32_e32 v192, v192
	v_rcp_f32_e32 v193, v193
	s_nop 0
	v_pk_mul_f32 v[180:181], v[180:181], v[192:193]
	s_nop 0
	v_pk_fma_f32 v[190:191], v[180:181], v[190:191], v[180:181]
	v_cvt_pk_bf16_f32 v180, v166, v167
	v_lshlrev_b64 v[166:167], 11, v[164:165]
	v_cvt_pk_bf16_f32 v181, v182, v183
	v_cvt_pk_bf16_f32 v182, v188, v189
	v_lshl_add_u64 v[188:189], s[28:29], 0, v[166:167]
	v_lshlrev_b64 v[166:167], 1, v[162:163]
	v_lshl_add_u64 v[162:163], v[188:189], 0, v[166:167]
	v_cvt_pk_bf16_f32 v183, v190, v191
	s_waitcnt vmcnt(0)
	global_store_dwordx4 v[162:163], v[180:183], off
	s_nop 1
	v_med3_f32 v180, v106, s57, v234
	v_med3_f32 v181, v107, s57, v234
	v_pk_mul_f32 v[188:189], v[180:181], s[96:97] op_sel_hi:[1,0]
	v_med3_f32 v182, v70, s33, v234
	v_exp_f32_e32 v188, v188
	v_exp_f32_e32 v189, v189
	v_med3_f32 v183, v71, s33, v234
	v_pk_add_f32 v[188:189], v[188:189], 1.0 op_sel_hi:[1,0]
	s_nop 0
	v_rcp_f32_e32 v188, v188
	v_rcp_f32_e32 v189, v189
	s_nop 0
	v_pk_mul_f32 v[180:181], v[180:181], v[188:189]
	s_nop 0
	v_pk_fma_f32 v[180:181], v[180:181], v[182:183], v[180:181]
	v_med3_f32 v182, v108, s57, v234
	v_med3_f32 v183, v109, s57, v234
	v_pk_mul_f32 v[190:191], v[182:183], s[96:97] op_sel_hi:[1,0]
	v_med3_f32 v188, v72, s33, v234
	v_exp_f32_e32 v190, v190
	v_exp_f32_e32 v191, v191
	v_med3_f32 v189, v73, s33, v234
	v_cvt_pk_bf16_f32 v180, v180, v181
	v_pk_add_f32 v[190:191], v[190:191], 1.0 op_sel_hi:[1,0]
	s_nop 0
	v_rcp_f32_e32 v190, v190
	v_rcp_f32_e32 v191, v191
	s_nop 0
	v_pk_mul_f32 v[182:183], v[182:183], v[190:191]
	s_nop 0
	v_pk_fma_f32 v[182:183], v[182:183], v[188:189], v[182:183]
	v_med3_f32 v188, v98, s57, v234
	v_med3_f32 v189, v99, s57, v234
	v_pk_mul_f32 v[192:193], v[188:189], s[96:97] op_sel_hi:[1,0]
	v_med3_f32 v190, v66, s33, v234
	v_exp_f32_e32 v192, v192
	v_exp_f32_e32 v193, v193
	v_med3_f32 v191, v67, s33, v234
	v_cvt_pk_bf16_f32 v181, v182, v183
	v_pk_add_f32 v[192:193], v[192:193], 1.0 op_sel_hi:[1,0]
	s_nop 0
	v_rcp_f32_e32 v192, v192
	v_rcp_f32_e32 v193, v193
	s_nop 0
	v_pk_mul_f32 v[188:189], v[188:189], v[192:193]
	s_nop 0
	v_pk_fma_f32 v[188:189], v[188:189], v[190:191], v[188:189]
	v_med3_f32 v190, v100, s57, v234
	v_med3_f32 v191, v101, s57, v234
	v_pk_mul_f32 v[194:195], v[190:191], s[96:97] op_sel_hi:[1,0]
	v_cvt_pk_bf16_f32 v182, v188, v189
	v_or_b32_e32 v188, 16, v164
	v_exp_f32_e32 v194, v194
	v_exp_f32_e32 v195, v195
	v_ashrrev_i32_e32 v189, 31, v188
	v_lshlrev_b64 v[188:189], 11, v[188:189]
	v_lshl_add_u64 v[188:189], s[28:29], 0, v[188:189]
	v_pk_add_f32 v[194:195], v[194:195], 1.0 op_sel_hi:[1,0]
	v_med3_f32 v192, v68, s33, v234
	v_rcp_f32_e32 v194, v194
	v_rcp_f32_e32 v195, v195
	v_med3_f32 v193, v69, s33, v234
	v_lshl_add_u64 v[188:189], v[188:189], 0, v[166:167]
	v_pk_mul_f32 v[190:191], v[190:191], v[194:195]
	s_nop 0
	v_pk_fma_f32 v[190:191], v[190:191], v[192:193], v[190:191]
; __device__ __forceinline__ u32x4 pack8(const f32x4 v0, const f32x4 v1) { u32x4 w; w.x = cvt_pk_bf16(v0[0], v0[1]); w.y = cvt_pk_bf16(v0[2], v0[3]); w.z = cvt_pk_bf16(v1[0], v1[1]); w.w = cvt_pk_bf16(v1[2], v1[3]); return w; }
;     __device__ __forceinline__ void operator()(const f32x4 (&acc)[2][2][4][2], const Unit& u, int wr, int wc, int fr, int fq) const {
;     ...
;         for (int ai = 0; ai < 2; ++ai)
; #pragma unroll
;             for (int m = 0; m < 4; ++m) {
;                 f32x4 o[2];
; #pragma unroll
;                 for (int n = 0; n < 2; ++n) { const f32x4 g4 = acc[ai][0][m][n], u4 = acc[ai][1][m][n];
; #pragma unroll
;                     for (int i = 0; i < 4; i += 2) {
;                         typedef float f32x2p __attribute__((ext_vector_type(2)));
;                         const f32x2p g = {__builtin_amdgcn_fmed3f(g4[i], -3.0e38f, 7.0f), __builtin_amdgcn_fmed3f(g4[i + 1], -3.0e38f, 7.0f)}, up = {__builtin_amdgcn_fmed3f(u4[i], -7.0f, 7.0f), __builtin_amdgcn_fmed3f(u4[i + 1], -7.0f, 7.0f)};
;                         const f32x2p a = g * (f32x2p){-1.702f * 1.4426950408889634f, -1.702f * 1.4426950408889634f};
;                         const f32x2p d = (f32x2p){__builtin_amdgcn_exp2f(a.x), __builtin_amdgcn_exp2f(a.y)} + (f32x2p){1.0f, 1.0f};
;                         const f32x2p t = g * (f32x2p){__builtin_amdgcn_rcpf(d.x), __builtin_amdgcn_rcpf(d.y)};
;                         const f32x2p r = __builtin_elementwise_fma(t, up, t); o[n][i] = r.x; o[n][i + 1] = r.y; } }
;                 *(u32x4*)(ACT + (size_t)(row0 + ai * HALF + m * 16) * 1024 + f0) = pack8(o[0], o[1]); }
	s_nop 0
	v_cvt_pk_bf16_f32 v183, v190, v191
	global_store_dwordx4 v[188:189], v[180:183], off
	s_nop 1
	v_med3_f32 v180, v94, s57, v234
	v_med3_f32 v181, v95, s57, v234
	v_pk_mul_f32 v[188:189], v[180:181], s[96:97] op_sel_hi:[1,0]
	v_med3_f32 v182, v62, s33, v234
	v_exp_f32_e32 v188, v188
	v_exp_f32_e32 v189, v189
	v_med3_f32 v183, v63, s33, v234
	v_pk_add_f32 v[188:189], v[188:189], 1.0 op_sel_hi:[1,0]
	s_nop 0
	v_rcp_f32_e32 v188, v188
	v_rcp_f32_e32 v189, v189
	s_nop 0
	v_pk_mul_f32 v[180:181], v[180:181], v[188:189]
	s_nop 0
	v_pk_fma_f32 v[180:181], v[180:181], v[182:183], v[180:181]
	v_med3_f32 v182, v96, s57, v234
	v_med3_f32 v183, v97, s57, v234
	v_pk_mul_f32 v[190:191], v[182:183], s[96:97] op_sel_hi:[1,0]
	v_med3_f32 v188, v64, s33, v234
	v_exp_f32_e32 v190, v190
	v_exp_f32_e32 v191, v191
	v_med3_f32 v189, v65, s33, v234
	v_cvt_pk_bf16_f32 v180, v180, v181
	v_pk_add_f32 v[190:191], v[190:191], 1.0 op_sel_hi:[1,0]
	s_nop 0
	v_rcp_f32_e32 v190, v190
	v_rcp_f32_e32 v191, v191
	s_nop 0
	v_pk_mul_f32 v[182:183], v[182:183], v[190:191]
	s_nop 0
	v_pk_fma_f32 v[182:183], v[182:183], v[188:189], v[182:183]
	v_med3_f32 v188, v90, s57, v234
	v_med3_f32 v189, v91, s57, v234
	v_pk_mul_f32 v[192:193], v[188:189], s[96:97] op_sel_hi:[1,0]
	v_med3_f32 v190, v58, s33, v234
	v_exp_f32_e32 v192, v192
	v_exp_f32_e32 v193, v193
	v_med3_f32 v191, v59, s33, v234
	v_cvt_pk_bf16_f32 v181, v182, v183
	v_pk_add_f32 v[192:193], v[192:193], 1.0 op_sel_hi:[1,0]
	s_nop 0
	v_rcp_f32_e32 v192, v192
	v_rcp_f32_e32 v193, v193
	s_nop 0
	v_pk_mul_f32 v[188:189], v[188:189], v[192:193]
	s_nop 0
	v_pk_fma_f32 v[188:189], v[188:189], v[190:191], v[188:189]
	v_med3_f32 v190, v92, s57, v234
	v_med3_f32 v191, v93, s57, v234
	v_pk_mul_f32 v[194:195], v[190:191], s[96:97] op_sel_hi:[1,0]
	v_cvt_pk_bf16_f32 v182, v188, v189
	v_or_b32_e32 v188, 32, v164
	v_exp_f32_e32 v194, v194
	v_exp_f32_e32 v195, v195
	v_ashrrev_i32_e32 v189, 31, v188
	v_lshlrev_b64 v[188:189], 11, v[188:189]
	v_lshl_add_u64 v[188:189], s[28:29], 0, v[188:189]
	v_pk_add_f32 v[194:195], v[194:195], 1.0 op_sel_hi:[1,0]
	v_med3_f32 v192, v60, s33, v234
	v_rcp_f32_e32 v194, v194
	v_rcp_f32_e32 v195, v195
	v_med3_f32 v193, v61, s33, v234
	v_lshl_add_u64 v[188:189], v[188:189], 0, v[166:167]
	v_or_b32_e32 v164, 48, v164
	v_pk_mul_f32 v[190:191], v[190:191], v[194:195]
	v_ashrrev_i32_e32 v165, 31, v164
	v_pk_fma_f32 v[190:191], v[190:191], v[192:193], v[190:191]
	v_lshlrev_b64 v[164:165], 11, v[164:165]
	v_cvt_pk_bf16_f32 v183, v190, v191
	global_store_dwordx4 v[188:189], v[180:183], off
	v_lshl_add_u64 v[164:165], s[28:29], 0, v[164:165]
	v_lshl_add_u64 v[164:165], v[164:165], 0, v[166:167]
	v_med3_f32 v180, v86, s57, v234
	v_med3_f32 v181, v87, s57, v234
	v_pk_mul_f32 v[188:189], v[180:181], s[96:97] op_sel_hi:[1,0]
	v_med3_f32 v182, v54, s33, v234
	v_exp_f32_e32 v188, v188
	v_exp_f32_e32 v189, v189
	v_med3_f32 v183, v55, s33, v234
	v_med3_f32 v166, v22, s33, v234
	v_med3_f32 v167, v23, s33, v234
	v_pk_add_f32 v[188:189], v[188:189], 1.0 op_sel_hi:[1,0]
	s_nop 0
	v_rcp_f32_e32 v188, v188
	v_rcp_f32_e32 v189, v189
	s_nop 0
	v_pk_mul_f32 v[180:181], v[180:181], v[188:189]
	s_nop 0
	v_pk_fma_f32 v[180:181], v[180:181], v[182:183], v[180:181]
	v_med3_f32 v182, v88, s57, v234
	v_med3_f32 v183, v89, s57, v234
	v_pk_mul_f32 v[190:191], v[182:183], s[96:97] op_sel_hi:[1,0]
	v_med3_f32 v188, v56, s33, v234
	v_exp_f32_e32 v190, v190
	v_exp_f32_e32 v191, v191
	v_med3_f32 v189, v57, s33, v234
	v_cvt_pk_bf16_f32 v180, v180, v181
	v_pk_add_f32 v[190:191], v[190:191], 1.0 op_sel_hi:[1,0]
	s_nop 0
	v_rcp_f32_e32 v190, v190
	v_rcp_f32_e32 v191, v191
	s_nop 0
	v_pk_mul_f32 v[182:183], v[182:183], v[190:191]
	s_nop 0
	v_pk_fma_f32 v[182:183], v[182:183], v[188:189], v[182:183]
	v_med3_f32 v188, v82, s57, v234
	v_med3_f32 v189, v83, s57, v234
	v_pk_mul_f32 v[192:193], v[188:189], s[96:97] op_sel_hi:[1,0]
	v_med3_f32 v190, v50, s33, v234
	v_exp_f32_e32 v192, v192
	v_exp_f32_e32 v193, v193
	v_med3_f32 v191, v51, s33, v234
	v_cvt_pk_bf16_f32 v181, v182, v183
	v_pk_add_f32 v[192:193], v[192:193], 1.0 op_sel_hi:[1,0]
	s_nop 0
	v_rcp_f32_e32 v192, v192
	v_rcp_f32_e32 v193, v193
	s_nop 0
	v_pk_mul_f32 v[188:189], v[188:189], v[192:193]
	s_nop 0
	v_pk_fma_f32 v[188:189], v[188:189], v[190:191], v[188:189]
	v_med3_f32 v190, v84, s57, v234
	v_med3_f32 v191, v85, s57, v234
	v_pk_mul_f32 v[194:195], v[190:191], s[96:97] op_sel_hi:[1,0]
	v_med3_f32 v192, v52, s33, v234
	v_exp_f32_e32 v194, v194
	v_exp_f32_e32 v195, v195
	v_med3_f32 v193, v53, s33, v234
	v_cvt_pk_bf16_f32 v182, v188, v189
	v_pk_add_f32 v[194:195], v[194:195], 1.0 op_sel_hi:[1,0]
	s_nop 0
	v_rcp_f32_e32 v194, v194
	v_rcp_f32_e32 v195, v195
	s_nop 0
	v_pk_mul_f32 v[190:191], v[190:191], v[194:195]
	s_nop 0
	v_pk_fma_f32 v[190:191], v[190:191], v[192:193], v[190:191]
	s_nop 0
	v_cvt_pk_bf16_f32 v183, v190, v191
	global_store_dwordx4 v[164:165], v[180:183], off
	v_med3_f32 v164, v46, s57, v234
	v_med3_f32 v165, v47, s57, v234
	v_pk_mul_f32 v[180:181], v[164:165], s[96:97] op_sel_hi:[1,0]
	s_nop 0
	v_exp_f32_e32 v180, v180
	v_exp_f32_e32 v181, v181
	s_nop 0
	v_pk_add_f32 v[180:181], v[180:181], 1.0 op_sel_hi:[1,0]
	s_nop 0
	v_rcp_f32_e32 v180, v180
	v_rcp_f32_e32 v181, v181
	s_nop 0
	v_pk_mul_f32 v[164:165], v[164:165], v[180:181]
	s_nop 0
	v_pk_fma_f32 v[164:165], v[164:165], v[166:167], v[164:165]
	v_med3_f32 v166, v48, s57, v234
	v_med3_f32 v167, v49, s57, v234
	v_pk_mul_f32 v[182:183], v[166:167], s[96:97] op_sel_hi:[1,0]
	v_med3_f32 v180, v24, s33, v234
	v_exp_f32_e32 v182, v182
	v_exp_f32_e32 v183, v183
	v_med3_f32 v181, v25, s33, v234
	v_cvt_pk_bf16_f32 v164, v164, v165
; __device__ __forceinline__ u32x4 pack8(const f32x4 v0, const f32x4 v1) { u32x4 w; w.x = cvt_pk_bf16(v0[0], v0[1]); w.y = cvt_pk_bf16(v0[2], v0[3]); w.z = cvt_pk_bf16(v1[0], v1[1]); w.w = cvt_pk_bf16(v1[2], v1[3]); return w; }
;     __device__ __forceinline__ void operator()(const f32x4 (&acc)[2][2][4][2], const Unit& u, int wr, int wc, int fr, int fq) const {
;     ...
;         for (int ai = 0; ai < 2; ++ai)
; #pragma unroll
;             for (int m = 0; m < 4; ++m) {
;                 f32x4 o[2];
; #pragma unroll
;                 for (int n = 0; n < 2; ++n) { const f32x4 g4 = acc[ai][0][m][n], u4 = acc[ai][1][m][n];
; #pragma unroll
;                     for (int i = 0; i < 4; i += 2) {
;                         typedef float f32x2p __attribute__((ext_vector_type(2)));
;                         const f32x2p g = {__builtin_amdgcn_fmed3f(g4[i], -3.0e38f, 7.0f), __builtin_amdgcn_fmed3f(g4[i + 1], -3.0e38f, 7.0f)}, up = {__builtin_amdgcn_fmed3f(u4[i], -7.0f, 7.0f), __builtin_amdgcn_fmed3f(u4[i + 1], -7.0f, 7.0f)};
;                         const f32x2p a = g * (f32x2p){-1.702f * 1.4426950408889634f, -1.702f * 1.4426950408889634f};
;                         const f32x2p d = (f32x2p){__builtin_amdgcn_exp2f(a.x), __builtin_amdgcn_exp2f(a.y)} + (f32x2p){1.0f, 1.0f};
;                         const f32x2p t = g * (f32x2p){__builtin_amdgcn_rcpf(d.x), __builtin_amdgcn_rcpf(d.y)};
;                         const f32x2p r = __builtin_elementwise_fma(t, up, t); o[n][i] = r.x; o[n][i + 1] = r.y; } }
;                 *(u32x4*)(ACT + (size_t)(row0 + ai * HALF + m * 16) * 1024 + f0) = pack8(o[0], o[1]); }
	v_pk_add_f32 v[182:183], v[182:183], 1.0 op_sel_hi:[1,0]
	s_nop 0
	v_rcp_f32_e32 v182, v182
	v_rcp_f32_e32 v183, v183
	s_nop 0
	v_pk_mul_f32 v[166:167], v[166:167], v[182:183]
	s_nop 0
	v_pk_fma_f32 v[166:167], v[166:167], v[180:181], v[166:167]
	v_med3_f32 v180, v42, s57, v234
	v_med3_f32 v181, v43, s57, v234
	v_pk_mul_f32 v[188:189], v[180:181], s[96:97] op_sel_hi:[1,0]
	v_med3_f32 v182, v18, s33, v234
	v_exp_f32_e32 v188, v188
	v_exp_f32_e32 v189, v189
	v_med3_f32 v183, v19, s33, v234
	v_cvt_pk_bf16_f32 v165, v166, v167
	v_pk_add_f32 v[188:189], v[188:189], 1.0 op_sel_hi:[1,0]
	s_nop 0
	v_rcp_f32_e32 v188, v188
	v_rcp_f32_e32 v189, v189
	s_nop 0
	v_pk_mul_f32 v[180:181], v[180:181], v[188:189]
	s_nop 0
	v_pk_fma_f32 v[180:181], v[180:181], v[182:183], v[180:181]
	v_med3_f32 v182, v44, s57, v234
	v_med3_f32 v183, v45, s57, v234
	v_pk_mul_f32 v[190:191], v[182:183], s[96:97] op_sel_hi:[1,0]
	v_cvt_pk_bf16_f32 v166, v180, v181
	v_add_co_u32_e32 v180, vcc, s2, v162
	v_exp_f32_e32 v190, v190
	v_exp_f32_e32 v191, v191
	v_med3_f32 v188, v20, s33, v234
	v_med3_f32 v189, v21, s33, v234
	v_addc_co_u32_e32 v181, vcc, 0, v163, vcc
	v_pk_add_f32 v[190:191], v[190:191], 1.0 op_sel_hi:[1,0]
	s_mov_b32 s2, 0x48000
	v_rcp_f32_e32 v190, v190
	v_rcp_f32_e32 v191, v191
	s_nop 0
	v_pk_mul_f32 v[182:183], v[182:183], v[190:191]
	s_nop 0
	v_pk_fma_f32 v[182:183], v[182:183], v[188:189], v[182:183]
	s_nop 0
	v_cvt_pk_bf16_f32 v167, v182, v183
	global_store_dwordx4 v[180:181], v[164:167], off
	s_nop 1
	v_med3_f32 v164, v38, s57, v234
	v_med3_f32 v165, v39, s57, v234
	v_pk_mul_f32 v[180:181], v[164:165], s[96:97] op_sel_hi:[1,0]
	v_med3_f32 v166, v14, s33, v234
	v_exp_f32_e32 v180, v180
	v_exp_f32_e32 v181, v181
	v_med3_f32 v167, v15, s33, v234
	v_pk_add_f32 v[180:181], v[180:181], 1.0 op_sel_hi:[1,0]
	s_nop 0
	v_rcp_f32_e32 v180, v180
	v_rcp_f32_e32 v181, v181
	s_nop 0
	v_pk_mul_f32 v[164:165], v[164:165], v[180:181]
	s_nop 0
	v_pk_fma_f32 v[164:165], v[164:165], v[166:167], v[164:165]
	v_med3_f32 v166, v40, s57, v234
	v_med3_f32 v167, v41, s57, v234
	v_pk_mul_f32 v[182:183], v[166:167], s[96:97] op_sel_hi:[1,0]
	v_med3_f32 v180, v16, s33, v234
	v_exp_f32_e32 v182, v182
	v_exp_f32_e32 v183, v183
	v_med3_f32 v181, v17, s33, v234
	v_cvt_pk_bf16_f32 v164, v164, v165
	v_pk_add_f32 v[182:183], v[182:183], 1.0 op_sel_hi:[1,0]
	s_nop 0
	v_rcp_f32_e32 v182, v182
	v_rcp_f32_e32 v183, v183
	s_nop 0
	v_pk_mul_f32 v[166:167], v[166:167], v[182:183]
	s_nop 0
	v_pk_fma_f32 v[166:167], v[166:167], v[180:181], v[166:167]
	v_med3_f32 v180, v34, s57, v234
	v_med3_f32 v181, v35, s57, v234
	v_pk_mul_f32 v[188:189], v[180:181], s[96:97] op_sel_hi:[1,0]
	v_med3_f32 v182, v10, s33, v234
	v_exp_f32_e32 v188, v188
	v_exp_f32_e32 v189, v189
	v_med3_f32 v183, v11, s33, v234
	v_cvt_pk_bf16_f32 v165, v166, v167
	v_pk_add_f32 v[188:189], v[188:189], 1.0 op_sel_hi:[1,0]
	s_nop 0
	v_rcp_f32_e32 v188, v188
	v_rcp_f32_e32 v189, v189
	s_nop 0
	v_pk_mul_f32 v[180:181], v[180:181], v[188:189]
	s_nop 0
	v_pk_fma_f32 v[180:181], v[180:181], v[182:183], v[180:181]
	v_med3_f32 v182, v36, s57, v234
	v_med3_f32 v183, v37, s57, v234
	v_pk_mul_f32 v[190:191], v[182:183], s[96:97] op_sel_hi:[1,0]
	v_cvt_pk_bf16_f32 v166, v180, v181
	v_add_co_u32_e32 v180, vcc, s2, v162
	v_exp_f32_e32 v190, v190
	v_exp_f32_e32 v191, v191
	v_med3_f32 v188, v12, s33, v234
	v_med3_f32 v189, v13, s33, v234
	v_addc_co_u32_e32 v181, vcc, 0, v163, vcc
	v_pk_add_f32 v[190:191], v[190:191], 1.0 op_sel_hi:[1,0]
	s_mov_b32 s2, 0x50000
	v_rcp_f32_e32 v190, v190
	v_rcp_f32_e32 v191, v191
	s_nop 0
	v_pk_mul_f32 v[182:183], v[182:183], v[190:191]
	s_nop 0
	v_pk_fma_f32 v[182:183], v[182:183], v[188:189], v[182:183]
	s_nop 0
	v_cvt_pk_bf16_f32 v167, v182, v183
	global_store_dwordx4 v[180:181], v[164:167], off
	s_nop 1
	v_med3_f32 v164, v30, s57, v234
	v_med3_f32 v165, v31, s57, v234
	v_pk_mul_f32 v[180:181], v[164:165], s[96:97] op_sel_hi:[1,0]
	v_med3_f32 v166, v102, s33, v234
	v_exp_f32_e32 v180, v180
	v_exp_f32_e32 v181, v181
	v_med3_f32 v167, v103, s33, v234
	v_pk_add_f32 v[180:181], v[180:181], 1.0 op_sel_hi:[1,0]
	s_nop 0
	v_rcp_f32_e32 v180, v180
	v_rcp_f32_e32 v181, v181
	s_nop 0
	v_pk_mul_f32 v[164:165], v[164:165], v[180:181]
	s_nop 0
; __device__ __forceinline__ u32x4 pack8(const f32x4 v0, const f32x4 v1) { u32x4 w; w.x = cvt_pk_bf16(v0[0], v0[1]); w.y = cvt_pk_bf16(v0[2], v0[3]); w.z = cvt_pk_bf16(v1[0], v1[1]); w.w = cvt_pk_bf16(v1[2], v1[3]); return w; }
; #define PG8_BAR __builtin_amdgcn_s_barrier()
;     __device__ __forceinline__ void operator()(const f32x4 (&acc)[2][2][4][2], const Unit& u, int wr, int wc, int fr, int fq) const {
;     ...
;         for (int ai = 0; ai < 2; ++ai)
; #pragma unroll
;             for (int m = 0; m < 4; ++m) {
;                 f32x4 o[2];
; #pragma unroll
;                 for (int n = 0; n < 2; ++n) { const f32x4 g4 = acc[ai][0][m][n], u4 = acc[ai][1][m][n];
; #pragma unroll
;                     for (int i = 0; i < 4; i += 2) {
;                         typedef float f32x2p __attribute__((ext_vector_type(2)));
;                         const f32x2p g = {__builtin_amdgcn_fmed3f(g4[i], -3.0e38f, 7.0f), __builtin_amdgcn_fmed3f(g4[i + 1], -3.0e38f, 7.0f)}, up = {__builtin_amdgcn_fmed3f(u4[i], -7.0f, 7.0f), __builtin_amdgcn_fmed3f(u4[i + 1], -7.0f, 7.0f)};
;                         const f32x2p a = g * (f32x2p){-1.702f * 1.4426950408889634f, -1.702f * 1.4426950408889634f};
;                         const f32x2p d = (f32x2p){__builtin_amdgcn_exp2f(a.x), __builtin_amdgcn_exp2f(a.y)} + (f32x2p){1.0f, 1.0f};
;                         const f32x2p t = g * (f32x2p){__builtin_amdgcn_rcpf(d.x), __builtin_amdgcn_rcpf(d.y)};
;                         const f32x2p r = __builtin_elementwise_fma(t, up, t); o[n][i] = r.x; o[n][i + 1] = r.y; } }
;                 *(u32x4*)(ACT + (size_t)(row0 + ai * HALF + m * 16) * 1024 + f0) = pack8(o[0], o[1]); }
; template <class Epi, class Sched, bool ALIGN_EPI = false, bool SP2 = false, bool GATHER = false>
; __device__ __forceinline__ void gemm_phase(PG8_LAS unsigned char* lds, const Gemm g, const Sched& S, const Epi& E, const int2* gslot = nullptr, PG8_LAS unsigned char* gtab = nullptr) {
;     ...
;         if constexpr (!Epi::AFTER_DRAIN) { E(acc, cur, wr, wc, fr, fq); S.done(cur); }
;         if (!has_next) break;
;         E.init(acc, pre);
;         cur = nxt; cA = nA; cB = nB; ++ui;
;         if constexpr (GATHER) { _Pragma("unroll") for (int h_ = 0; h_ < 2; ++h_) _Pragma("unroll") for (int i_ = 0; i_ < 2; ++i_) vC[h_][i_] = vN[h_][i_]; }
;         if constexpr (ALIGN_EPI) { if (wr == 1) PG8_BAR; }
	v_pk_fma_f32 v[164:165], v[164:165], v[166:167], v[164:165]
	v_med3_f32 v166, v32, s57, v234
	v_med3_f32 v167, v33, s57, v234
	v_pk_mul_f32 v[182:183], v[166:167], s[96:97] op_sel_hi:[1,0]
	v_med3_f32 v180, v104, s33, v234
	v_exp_f32_e32 v182, v182
	v_exp_f32_e32 v183, v183
	v_med3_f32 v181, v105, s33, v234
	v_cvt_pk_bf16_f32 v164, v164, v165
	v_pk_add_f32 v[182:183], v[182:183], 1.0 op_sel_hi:[1,0]
	s_nop 0
	v_rcp_f32_e32 v182, v182
	v_rcp_f32_e32 v183, v183
	s_nop 0
	v_pk_mul_f32 v[166:167], v[166:167], v[182:183]
	s_nop 0
	v_pk_fma_f32 v[166:167], v[166:167], v[180:181], v[166:167]
	v_med3_f32 v180, v26, s57, v234
	v_med3_f32 v181, v27, s57, v234
	v_pk_mul_f32 v[188:189], v[180:181], s[96:97] op_sel_hi:[1,0]
	v_med3_f32 v182, v110, s33, v234
	v_exp_f32_e32 v188, v188
	v_exp_f32_e32 v189, v189
	v_med3_f32 v183, v111, s33, v234
	v_cvt_pk_bf16_f32 v165, v166, v167
	v_pk_add_f32 v[188:189], v[188:189], 1.0 op_sel_hi:[1,0]
	s_nop 0
	v_rcp_f32_e32 v188, v188
	v_rcp_f32_e32 v189, v189
	s_nop 0
	v_pk_mul_f32 v[180:181], v[180:181], v[188:189]
	s_nop 0
	v_pk_fma_f32 v[180:181], v[180:181], v[182:183], v[180:181]
	v_med3_f32 v182, v28, s57, v234
	v_med3_f32 v183, v29, s57, v234
	v_pk_mul_f32 v[190:191], v[182:183], s[96:97] op_sel_hi:[1,0]
	v_cvt_pk_bf16_f32 v166, v180, v181
	v_add_co_u32_e32 v180, vcc, s2, v162
	v_exp_f32_e32 v190, v190
	v_exp_f32_e32 v191, v191
	v_med3_f32 v188, v112, s33, v234
	v_med3_f32 v189, v113, s33, v234
	v_addc_co_u32_e32 v181, vcc, 0, v163, vcc
	v_pk_add_f32 v[190:191], v[190:191], 1.0 op_sel_hi:[1,0]
	v_add_co_u32_e32 v162, vcc, 0x58000, v162
	v_rcp_f32_e32 v190, v190
	v_rcp_f32_e32 v191, v191
	v_addc_co_u32_e32 v163, vcc, 0, v163, vcc
	s_and_b64 vcc, exec, s[6:7]
	v_pk_mul_f32 v[182:183], v[182:183], v[190:191]
	s_nop 0
	v_pk_fma_f32 v[182:183], v[182:183], v[188:189], v[182:183]
	s_nop 0
	v_cvt_pk_bf16_f32 v167, v182, v183
	global_store_dwordx4 v[180:181], v[164:167], off
	s_nop 1
	v_med3_f32 v164, v6, s57, v234
	v_med3_f32 v165, v7, s57, v234
	v_pk_mul_f32 v[180:181], v[164:165], s[96:97] op_sel_hi:[1,0]
	v_med3_f32 v166, v118, s33, v234
	v_exp_f32_e32 v180, v180
	v_exp_f32_e32 v181, v181
	v_med3_f32 v167, v119, s33, v234
	v_pk_add_f32 v[180:181], v[180:181], 1.0 op_sel_hi:[1,0]
	s_nop 0
	v_rcp_f32_e32 v180, v180
	v_rcp_f32_e32 v181, v181
	s_nop 0
	v_pk_mul_f32 v[164:165], v[164:165], v[180:181]
	s_nop 0
	v_pk_fma_f32 v[164:165], v[164:165], v[166:167], v[164:165]
	v_med3_f32 v166, v8, s57, v234
	v_med3_f32 v167, v9, s57, v234
	v_pk_mul_f32 v[182:183], v[166:167], s[96:97] op_sel_hi:[1,0]
	v_med3_f32 v180, v120, s33, v234
	v_exp_f32_e32 v182, v182
	v_exp_f32_e32 v183, v183
	v_med3_f32 v181, v121, s33, v234
	v_cvt_pk_bf16_f32 v164, v164, v165
	v_pk_add_f32 v[182:183], v[182:183], 1.0 op_sel_hi:[1,0]
	s_nop 0
	v_rcp_f32_e32 v182, v182
	v_rcp_f32_e32 v183, v183
	s_nop 0
	v_pk_mul_f32 v[166:167], v[166:167], v[182:183]
	s_nop 0
	v_pk_fma_f32 v[166:167], v[166:167], v[180:181], v[166:167]
	v_med3_f32 v180, v2, s57, v234
	v_med3_f32 v181, v3, s57, v234
	v_pk_mul_f32 v[188:189], v[180:181], s[96:97] op_sel_hi:[1,0]
	v_med3_f32 v182, v126, s33, v234
	v_exp_f32_e32 v188, v188
	v_exp_f32_e32 v189, v189
	v_med3_f32 v183, v127, s33, v234
	v_cvt_pk_bf16_f32 v165, v166, v167
	v_pk_add_f32 v[188:189], v[188:189], 1.0 op_sel_hi:[1,0]
	s_nop 0
	v_rcp_f32_e32 v188, v188
	v_rcp_f32_e32 v189, v189
	s_nop 0
	v_pk_mul_f32 v[180:181], v[180:181], v[188:189]
	s_nop 0
	v_pk_fma_f32 v[180:181], v[180:181], v[182:183], v[180:181]
	v_med3_f32 v182, v4, s57, v234
	v_med3_f32 v183, v5, s57, v234
	v_pk_mul_f32 v[190:191], v[182:183], s[96:97] op_sel_hi:[1,0]
	v_med3_f32 v188, v128, s33, v234
	v_exp_f32_e32 v190, v190
	v_exp_f32_e32 v191, v191
	v_med3_f32 v189, v129, s33, v234
	v_cvt_pk_bf16_f32 v166, v180, v181
	v_pk_add_f32 v[190:191], v[190:191], 1.0 op_sel_hi:[1,0]
	s_nop 0
	v_rcp_f32_e32 v190, v190
	v_rcp_f32_e32 v191, v191
	s_nop 0
	v_pk_mul_f32 v[182:183], v[182:183], v[190:191]
	s_nop 0
	v_pk_fma_f32 v[182:183], v[182:183], v[188:189], v[182:183]
	s_nop 0
	v_cvt_pk_bf16_f32 v167, v182, v183
	global_store_dwordx4 v[162:163], v[164:167], off
	s_cbranch_vccnz .LBB0_1102
	s_andn2_b64 vcc, exec, s[26:27]
	s_cbranch_vccnz .LBB0_1080
	s_barrier
	s_branch .LBB0_1080
